# v35 + waves 0-3 issue both K pieces behind the PV section too (no DMA between the barrier and the first QK MFMA)
# baseline (speedup 1.0000x reference)
; template <bool FOX>
; __device__ __forceinline__ void attn_unit(const Args& A, int b, int h, int qb, LAS char* shm, LAS float* dg) {
;     ...
;         if (t == 1 && 4 < nti) ISSUE_K(t0 + 4, 0);
;         if (t + 4 < nti) ISSUE_K(t0 + t + 4, t % NS);
;         if (t + 2 < nti) ISSUE_V(t0 + t + 2, (t + 2) % NS);
;         SFENCE();
;         { if constexpr (!FOX) { if (t0 + t == tw_last + 1) {
; #pragma unroll
;                   for (int r = 0; r < 16; ++r) negm[r] = -INFINITY;
;                   asm volatile("" : "+v"(negm)); } }
;           const lds_cptr vp = vp0 + ((t - 1) % NS) * VSLOT; float sa = 0.f, sb = 0.f;
; #pragma unroll
;           for (int g = 0; g < 2 * NQ; ++g) {
;               if (!FOX && g == 0) c0 = __builtin_amdgcn_mfma_f32_32x32x16_bf16(kf[0], qr[0], negm, 0, 0, 0);
;               else if (!FOX && g == 1) c1 = __builtin_amdgcn_mfma_f32_32x32x16_bf16(kf[1], qr[0], negm, 0, 0, 0);
;               else if (g & 1) c1 = __builtin_amdgcn_mfma_f32_32x32x16_bf16(kf[g], qr[g >> 1], c1, 0, 0, 0); else c0 = __builtin_amdgcn_mfma_f32_32x32x16_bf16(kf[g], qr[g >> 1], c0, 0, 0, 0);
;               if (g < 8) { const int i = (g >> 1) + 4 * (g & 1); vlo[i] = vtr(vp + (i >> 2) * 4096 + (i & 3) * 1024); vhi[i] = vtr(vp + (i >> 2) * 4096 + (i & 3) * 1024 + 512);
;                   if (g < 4) { sa += pp0[4 * g]; sb += pp0[4 * g + 1]; sa += pp0[4 * g + 2]; sb += pp0[4 * g + 3]; } else { sa += pp1[4 * g - 16]; sb += pp1[4 * g - 15]; sa += pp1[4 * g - 14]; sb += pp1[4 * g - 13]; }
;                   asm volatile("" : "+v"(sa), "+v"(sb)); }
;               { constexpr int G0 = FOX ? 0 : 4; if (g >= G0) { const int q = 2 * (g - G0);
; #pragma unroll
;                   for (int k = 0; k < 2; ++k) { const int w = q + k; const unsigned pkd = w < 8 ? cvt_pk_bf16(pp0[2 * w], pp0[2 * w + 1]) : cvt_pk_bf16(pp1[2 * w - 16], pp1[2 * w - 15]); pw[w >> 2][w & 3] = pkd; } } }
;               SFENCE();
;           }
;           lrun += sa + sb; }
;         MASKONLY(t);
;         float rm; ROWMAX(rm);
;         bool resc = false;
;         if (__any(rm > THR)) { const float dl = fmaxf(rm, 0.f); mhat += dl;
; #pragma unroll
;             for (int r = 0; r < 16; ++r) { c0[r] -= dl; c1[r] -= dl; }
;             if constexpr (!FOX) {
; #pragma unroll
;                 for (int r = 0; r < 16; ++r) negm[r] = -mhat;
;                 asm volatile("" : "+v"(negm)); }
.Lmla_ss1_in:
	s_waitcnt lgkmcnt(0)
	s_add_i32 s27, s42, 0x8000
	v_mfma_f32_32x32x16_bf16 v[114:129], v[206:209], v[138:141], v[82:97]
	s_and_b32 s27, s27, 0x6000
	s_add_u32 s42, s42, 0x2000
	s_addc_u32 s43, s43, 0
	v_add_u32_e32 v3, s27, v247
	ds_read_b64_tr_b16 v[206:207], v3 offset:49152
	ds_read_b64_tr_b16 v[208:209], v3 offset:49664
	v_add_f32_e32 v4, 0, v67
	v_add_f32_e32 v5, 0, v66
	v_add_f32_e32 v4, v69, v4
	v_add_f32_e32 v5, v68, v5
	v_mfma_f32_32x32x16_bf16 v[98:113], v[194:197], v[138:141], v[82:97]
	ds_read_b64_tr_b16 v[194:195], v3 offset:53248
	ds_read_b64_tr_b16 v[196:197], v3 offset:53760
	v_add_f32_e32 v4, v71, v4
	v_add_f32_e32 v5, v70, v5
	v_add_f32_e32 v4, v73, v4
	v_add_f32_e32 v5, v72, v5
	v_mfma_f32_32x32x16_bf16 v[114:129], v[202:205], v[142:145], v[114:129]
	ds_read_b64_tr_b16 v[202:203], v3 offset:50176
	ds_read_b64_tr_b16 v[204:205], v3 offset:50688
	v_add_f32_e32 v4, v75, v4
	v_add_f32_e32 v5, v74, v5
	v_add_f32_e32 v4, v77, v4
	v_add_f32_e32 v5, v76, v5
	v_mfma_f32_32x32x16_bf16 v[98:113], v[186:189], v[142:145], v[98:113]
	ds_read_b64_tr_b16 v[214:215], v3 offset:54272
	ds_read_b64_tr_b16 v[216:217], v3 offset:54784
	v_add_f32_e32 v4, v79, v4
	v_add_f32_e32 v5, v78, v5
	v_add_f32_e32 v4, v81, v4
	v_add_f32_e32 v5, v80, v5
	v_mfma_f32_32x32x16_bf16 v[114:129], v[198:201], v[146:149], v[114:129]
	ds_read_b64_tr_b16 v[210:211], v3 offset:51200
	ds_read_b64_tr_b16 v[212:213], v3 offset:51712
	v_add_f32_e32 v4, v51, v4
	v_add_f32_e32 v5, v50, v5
	v_add_f32_e32 v4, v53, v4
	v_add_f32_e32 v5, v52, v5
	v_mfma_f32_32x32x16_bf16 v[98:113], v[182:185], v[146:149], v[98:113]
	ds_read_b64_tr_b16 v[12:13], v3 offset:55296
	ds_read_b64_tr_b16 v[14:15], v3 offset:55808
	v_add_f32_e32 v4, v55, v4
	v_add_f32_e32 v5, v54, v5
	v_add_f32_e32 v4, v57, v4
	v_add_f32_e32 v5, v56, v5
	v_mfma_f32_32x32x16_bf16 v[114:129], v[190:193], v[150:153], v[114:129]
	ds_read_b64_tr_b16 v[8:9], v3 offset:52224
	ds_read_b64_tr_b16 v[10:11], v3 offset:52736
	v_add_f32_e32 v4, v59, v4
	v_add_f32_e32 v16, v61, v4
	v_add_f32_e32 v4, v58, v5
	v_add_f32_e32 v17, v60, v4
	v_mfma_f32_32x32x16_bf16 v[98:113], v[170:173], v[150:153], v[98:113]
	ds_read_b64_tr_b16 v[4:5], v3 offset:56320
	ds_read_b64_tr_b16 v[6:7], v3 offset:56832
	v_add_f32_e32 v3, v63, v16
	v_add_f32_e32 v16, v62, v17
	v_add_f32_e32 v3, v65, v3
	v_add_f32_e32 v16, v64, v16
	v_mfma_f32_32x32x16_bf16 v[114:129], v[178:181], v[154:157], v[114:129]
	v_cvt_pk_bf16_f32 v178, v50, v51
	v_cvt_pk_bf16_f32 v179, v52, v53
	v_cvt_pk_bf16_f32 v186, v66, v67
	v_cvt_pk_bf16_f32 v187, v68, v69
	v_mfma_f32_32x32x16_bf16 v[98:113], v[166:169], v[154:157], v[98:113]
	s_add_i32 s64, s42, 0x6000
	v_cvt_pk_bf16_f32 v180, v54, v55
	v_cvt_pk_bf16_f32 v181, v56, v57
	v_cvt_pk_bf16_f32 v188, v70, v71
	v_cvt_pk_bf16_f32 v189, v72, v73
	v_mfma_f32_32x32x16_bf16 v[114:129], v[174:177], v[158:161], v[114:129]
	s_and_b32 s64, s64, 0x6000
	s_add_i32 s65, s64, s93
	v_cvt_pk_bf16_f32 v218, v58, v59
	v_cvt_pk_bf16_f32 v219, v60, v61
	v_cvt_pk_bf16_f32 v182, v74, v75
	v_cvt_pk_bf16_f32 v183, v76, v77
	v_mfma_f32_32x32x16_bf16 v[98:113], v[162:165], v[158:161], v[98:113]
	v_cvt_pk_bf16_f32 v220, v62, v63
	v_cvt_pk_bf16_f32 v221, v64, v65
	v_cvt_pk_bf16_f32 v184, v78, v79
	v_cvt_pk_bf16_f32 v185, v80, v81
	v_add_f32_e32 v3, v3, v16
	v_add_f32_e32 v246, v246, v3
	s_nop 3
	s_waitcnt lgkmcnt(0)
	v_mfma_f32_32x32x16_bf16 v[18:33], v[186:189], v[206:209], v[18:33]
	s_add_i32 s27, s26, 1
	s_and_b32 s64, s27, 3
	s_mulk_i32 s64, 0x3000
	v_exp_f32_e32 v66, v114
	v_exp_f32_e32 v67, v115
	v_exp_f32_e32 v68, v116
	v_exp_f32_e32 v69, v117
	v_add_u32_e32 v3, s64, v248
	v_mfma_f32_32x32x16_bf16 v[34:49], v[186:189], v[194:197], v[34:49]
	v_exp_f32_e32 v70, v118
	v_exp_f32_e32 v71, v119
	v_exp_f32_e32 v72, v120
	v_exp_f32_e32 v73, v121
	ds_read_b128 v[206:209], v3
	ds_read_b128 v[194:197], v3 offset:512
	v_mfma_f32_32x32x16_bf16 v[18:33], v[182:185], v[202:205], v[18:33]
	v_exp_f32_e32 v74, v122
	v_exp_f32_e32 v75, v123
	v_exp_f32_e32 v76, v124
	v_exp_f32_e32 v77, v125
	ds_read_b128 v[202:205], v3 offset:2048
	ds_read_b128 v[186:189], v3 offset:2560
	v_mfma_f32_32x32x16_bf16 v[34:49], v[182:185], v[214:217], v[34:49]
	v_exp_f32_e32 v78, v126
	v_exp_f32_e32 v79, v127
	v_exp_f32_e32 v80, v128
	v_exp_f32_e32 v81, v129
	ds_read_b128 v[198:201], v3 offset:4096
	ds_read_b128 v[182:185], v3 offset:4608
	v_mfma_f32_32x32x16_bf16 v[18:33], v[178:181], v[210:213], v[18:33]
	v_exp_f32_e32 v50, v98
	v_exp_f32_e32 v51, v99
	v_exp_f32_e32 v52, v100
	v_exp_f32_e32 v53, v101
	ds_read_b128 v[190:193], v3 offset:6144
	ds_read_b128 v[170:173], v3 offset:6656
	v_mfma_f32_32x32x16_bf16 v[34:49], v[178:181], v[12:15], v[34:49]
	v_exp_f32_e32 v54, v102
	v_exp_f32_e32 v55, v103
	v_exp_f32_e32 v56, v104
	v_exp_f32_e32 v57, v105
	ds_read_b128 v[178:181], v3 offset:8192
	ds_read_b128 v[166:169], v3 offset:8704
	v_mfma_f32_32x32x16_bf16 v[18:33], v[218:221], v[8:11], v[18:33]
	v_exp_f32_e32 v58, v106
	v_exp_f32_e32 v59, v107
	v_exp_f32_e32 v60, v108
	v_exp_f32_e32 v61, v109
	ds_read_b128 v[174:177], v3 offset:10240
	ds_read_b128 v[162:165], v3 offset:10752
	v_mfma_f32_32x32x16_bf16 v[34:49], v[218:221], v[4:7], v[34:49]
	v_exp_f32_e32 v62, v110
	v_exp_f32_e32 v63, v111
	v_exp_f32_e32 v64, v112
	v_exp_f32_e32 v65, v113
	s_mov_b32 m0, s52
	s_and_b32 s64, s26, 3
	global_load_lds_dwordx4 v240, s[46:47]
	s_add_i32 m0, s52, 0x2000
	s_mulk_i32 s64, 0x3000
	global_load_lds_dwordx4 v240, s[98:99]
	s_mov_b32 m0, s53
	s_mov_b32 s53, s65
	global_load_lds_dwordx4 v240, s[60:61]
	s_add_i32 s52, s64, s91
	s_add_u32 s46, s46, s62
	s_addc_u32 s47, s47, s63
	s_add_u32 s98, s98, s62
	s_addc_u32 s99, s99, s63
	s_add_u32 s60, s60, 0x2000
	s_addc_u32 s61, s61, 0
	s_mov_b32 s26, s27
	s_cmp_eq_u32 s27, s96
	s_cbranch_scc1 .Lmla_ss1_xdone
	s_add_i32 s64, s27, 3
	s_cmp_lt_u32 s64, s94
	s_cbranch_scc1 .Lmla_ss1_top
	s_waitcnt vmcnt(4)
	s_barrier
	s_branch .Lmla_ss_back
